# v74 stack (without the later P4/P5/quantizer-shuffle extras, which showed two intermittent measure failures) with the P2 split back at 160 GEMM workgroups
# speedup vs baseline: 1.0034x; 1.0034x over previous
; #define LAS __attribute__((address_space(3)))
;     ...
; #pragma unroll
;         for (int g = 0; g < 8; ++g)
; #pragma unroll
;             for (int r = 0; r < 4; ++r) { mx[0] = fmaxf(mx[0], fabsf(v[g][r][0])); mx[1] = fmaxf(mx[1], fabsf(v[g][r][1])); mx[2] = fmaxf(mx[2], fabsf(v[g][r][2])); mx[3] = fmaxf(mx[3], fabsf(v[g][r][3])); }
; #pragma unroll
;         for (int c = 0; c < 4; ++c) { float m = mx[c]; m = fmaxf(m, __shfl_xor(m, 8)); m = fmaxf(m, __shfl_xor(m, 16)); m = fmaxf(m, __shfl_xor(m, 32)); mx[c] = m; }
;         if (tid == 0) MISC[2] = nxt;
;         if (kr == 0) *(LAS f32x4*)(smax + wave * 32 + 4 * n4) = mx;
.LBB0_334:
	s_waitcnt vmcnt(10)
	v_max3_f32 v130, |v2|, 0, |v6|
	s_waitcnt vmcnt(8)
	v_max3_f32 v130, v130, |v10|, |v14|
	v_max3_f32 v130, v130, |v18|, |v22|
	v_max3_f32 v130, v130, |v26|, |v30|
	v_max3_f32 v130, v130, |v34|, |v38|
	v_max3_f32 v130, v130, |v42|, |v46|
	v_max3_f32 v131, |v3|, 0, |v7|
	v_max3_f32 v130, v130, |v50|, |v54|
	v_max3_f32 v132, |v4|, 0, |v8|
	v_max3_f32 v131, v131, |v11|, |v15|
	v_max3_f32 v130, v130, |v58|, |v62|
	v_max3_f32 v132, v132, |v12|, |v16|
	v_max3_f32 v131, v131, |v19|, |v23|
	v_max3_f32 v130, v130, |v66|, |v70|
	v_max3_f32 v132, v132, |v20|, |v24|
	v_max3_f32 v131, v131, |v27|, |v31|
	v_max3_f32 v130, v130, |v74|, |v78|
	v_max3_f32 v132, v132, |v28|, |v32|
	v_max3_f32 v131, v131, |v35|, |v39|
	v_max3_f32 v130, v130, |v82|, |v86|
	v_max3_f32 v132, v132, |v36|, |v40|
	v_max3_f32 v131, v131, |v43|, |v47|
	v_max3_f32 v130, v130, |v90|, |v94|
	v_max3_f32 v132, v132, |v44|, |v48|
	v_max3_f32 v131, v131, |v51|, |v55|
	s_waitcnt vmcnt(6)
	v_max3_f32 v130, v130, |v98|, |v102|
	v_max3_f32 v133, |v5|, 0, |v9|
	v_max3_f32 v132, v132, |v52|, |v56|
	v_max3_f32 v131, v131, |v59|, |v63|
	s_waitcnt vmcnt(4)
	v_max3_f32 v130, v130, |v106|, |v110|
	v_max3_f32 v133, v133, |v13|, |v17|
	v_max3_f32 v132, v132, |v60|, |v64|
	v_max3_f32 v131, v131, |v67|, |v71|
	s_waitcnt vmcnt(2)
	v_max3_f32 v130, v130, |v114|, |v118|
	v_max3_f32 v133, v133, |v21|, |v25|
	v_max3_f32 v132, v132, |v68|, |v72|
	v_max3_f32 v131, v131, |v75|, |v79|
	s_waitcnt vmcnt(0)
	v_max3_f32 v130, v130, |v122|, |v126|
	v_max3_f32 v133, v133, |v29|, |v33|
	v_max3_f32 v132, v132, |v76|, |v80|
	v_max3_f32 v131, v131, |v83|, |v87|
	ds_bpermute_b32 v134, v163, v130
	v_max3_f32 v133, v133, |v37|, |v41|
	v_max3_f32 v132, v132, |v84|, |v88|
	v_max3_f32 v131, v131, |v91|, |v95|
	v_max3_f32 v133, v133, |v45|, |v49|
	v_max3_f32 v132, v132, |v92|, |v96|
	v_max3_f32 v131, v131, |v99|, |v103|
	v_max3_f32 v133, v133, |v53|, |v57|
	v_max3_f32 v132, v132, |v100|, |v104|
	v_max3_f32 v131, v131, |v107|, |v111|
	v_max3_f32 v133, v133, |v61|, |v65|
	v_max3_f32 v132, v132, |v108|, |v112|
	v_max3_f32 v131, v131, |v115|, |v119|
	v_max3_f32 v133, v133, |v69|, |v73|
	v_max3_f32 v132, v132, |v116|, |v120|
	v_max3_f32 v131, v131, |v123|, |v127|
	s_waitcnt lgkmcnt(0)
	v_max_f32_e32 v134, v134, v134
	v_max3_f32 v133, v133, |v77|, |v81|
	v_max3_f32 v135, v132, |v124|, |v128|
	ds_bpermute_b32 v132, v163, v131
	v_max_f32_e32 v130, v130, v134
	v_max3_f32 v133, v133, |v85|, |v89|
	ds_bpermute_b32 v134, v165, v130
	v_max3_f32 v133, v133, |v93|, |v97|
	v_max3_f32 v133, v133, |v101|, |v105|
	v_max3_f32 v133, v133, |v109|, |v113|
	v_max3_f32 v133, v133, |v117|, |v121|
	s_waitcnt lgkmcnt(1)
	v_max_f32_e32 v132, v132, v132
	v_max3_f32 v133, v133, |v125|, |v129|
	v_max_f32_e32 v132, v131, v132
	s_waitcnt lgkmcnt(0)
	v_max_f32_e32 v131, v134, v134
	ds_bpermute_b32 v134, v163, v135
	ds_bpermute_b32 v136, v165, v132
	ds_bpermute_b32 v137, v163, v133
	v_max_f32_e32 v130, v130, v131
	ds_bpermute_b32 v131, v167, v130
	s_waitcnt lgkmcnt(3)
	v_max_f32_e32 v134, v134, v134
	s_waitcnt lgkmcnt(2)
	v_max_f32_e32 v136, v136, v136
	v_max_f32_e32 v134, v135, v134
	s_waitcnt lgkmcnt(1)
	v_max_f32_e32 v135, v137, v137
	v_max_f32_e32 v132, v132, v136
	ds_bpermute_b32 v136, v165, v134
	v_max_f32_e32 v137, v133, v135
	ds_bpermute_b32 v138, v165, v137
	ds_bpermute_b32 v135, v167, v132
	s_waitcnt lgkmcnt(2)
	v_max_f32_e32 v133, v136, v136
	v_max_f32_e32 v133, v134, v133
	s_waitcnt lgkmcnt(1)
	v_max_f32_e32 v134, v138, v138
	v_max_f32_e32 v134, v137, v134
	ds_bpermute_b32 v136, v167, v133
	ds_bpermute_b32 v137, v167, v134
	s_and_saveexec_b64 s[6:7], s[40:41]
	v_add_u32_e32 v1, 0x1c8, v199
	v_cmp_lt_u32_e32 vcc, 55, v201
	s_mov_b64 s[12:13], vcc
	v_cmp_le_u32_e32 vcc, 0x19c8, v1
	s_or_b64 s[12:13], s[12:13], vcc
	v_mov_b32_e32 v199, 0x1800
	s_andn2_b64 exec, exec, s[12:13]
	v_mov_b32_e32 v203, 1
	global_atomic_add v199, v171, v203, s[20:21] sc0
	s_and_b64 exec, s[6:7], s[40:41]
	global_load_dword v201, v171, s[22:23] sc1
	v_mov_b32_e32 v138, s75
	ds_write_b32 v138, v1
	s_or_b64 exec, exec, s[6:7]
	s_and_saveexec_b64 s[6:7], s[4:5]
	s_cbranch_execz .LBB0_343
	v_max_f32_e32 v1, v131, v131
	v_max_f32_e32 v130, v130, v130
	v_max_f32_e32 v130, v130, v1
	s_waitcnt lgkmcnt(2)
	v_max_f32_e32 v1, v135, v135
	v_max_f32_e32 v131, v132, v132
	v_max_f32_e32 v131, v131, v1
	s_waitcnt lgkmcnt(1)
	v_max_f32_e32 v1, v136, v136
	v_max_f32_e32 v132, v133, v133
	v_max_f32_e32 v132, v132, v1
	s_waitcnt lgkmcnt(0)
	v_max_f32_e32 v1, v137, v137
	v_max_f32_e32 v133, v134, v134
	v_max_f32_e32 v133, v133, v1
	v_add_u32_e32 v1, s44, v169
	ds_write_b128 v1, v[130:133]
